# speedup vs baseline: 1.0021x; 1.0014x over previous
.Lout_P:
	s_waitcnt vmcnt(3) lgkmcnt(0)
	s_barrier
	s_setprio 0
	s_add_u32 s34, s20, s28
	s_addc_u32 s35, s21, s27
	s_waitcnt lgkmcnt(3)
	v_mfma_f32_16x16x32_f16 v[92:95], v[20:23], v[28:31], v[92:95]
	v_mfma_f32_16x16x32_f16 v[72:75], v[20:23], v[24:27], v[72:75]
	s_mov_b32 m0, s46
	s_nop 0
	global_load_lds_dwordx4 v100, s[14:15]
	v_mfma_f32_16x16x32_f16 v[56:59], v[20:23], v[16:19], v[56:59]
	v_mfma_f32_16x16x32_f16 v[20:23], v[20:23], v[0:3], v[40:43]
	s_mov_b32 m0, s47
	s_nop 0
	global_load_lds_dwordx4 v99, s[14:15]
	s_waitcnt lgkmcnt(2)
	v_mfma_f32_16x16x32_f16 v[88:91], v[12:15], v[28:31], v[88:91]
	s_mov_b32 m0, s51
	s_nop 0
	global_load_lds_dwordx4 v102, s[34:35]
	s_waitcnt lgkmcnt(1)
	v_mfma_f32_16x16x32_f16 v[80:83], v[8:11], v[28:31], v[80:83]
	s_waitcnt lgkmcnt(0)
	v_mfma_f32_16x16x32_f16 v[28:31], v[4:7], v[28:31], v[76:79]
	s_add_u32 s30, s14, 0x80000
	s_addc_u32 s31, s15, 0
	s_add_u32 s34, s20, s18
	v_mfma_f32_16x16x32_f16 v[68:71], v[12:15], v[24:27], v[68:71]
	s_addc_u32 s35, s21, s19
	v_mfma_f32_16x16x32_f16 v[64:67], v[8:11], v[24:27], v[64:67]
	v_mfma_f32_16x16x32_f16 v[24:27], v[4:7], v[24:27], v[60:63]
	v_mfma_f32_16x16x32_f16 v[48:51], v[12:15], v[16:19], v[48:51]
	v_mfma_f32_16x16x32_f16 v[52:55], v[8:11], v[16:19], v[52:55]
	v_mfma_f32_16x16x32_f16 v[16:19], v[4:7], v[16:19], v[44:47]
	v_mfma_f32_16x16x32_f16 v[36:39], v[12:15], v[0:3], v[36:39]
	v_mfma_f32_16x16x32_f16 v[32:35], v[8:11], v[0:3], v[32:35]
	v_mfma_f32_16x16x32_f16 v[84:87], v[4:7], v[0:3], v[84:87]
	s_setprio 1
	ds_read_b128 v[0:3], v103 offset:40960
	ds_read_b128 v[4:7], v103 offset:41984
	ds_read_b128 v[8:11], v98 offset:24576
	ds_read_b128 v[12:15], v98 offset:25600
	ds_read_b128 v[104:107], v103 offset:43008
	ds_read_b128 v[108:111], v103 offset:44032
	s_waitcnt lgkmcnt(3)
	v_mfma_f32_16x16x32_f16 v[92:95], v[0:3], v[8:11], v[92:95]
	v_mfma_f32_16x16x32_f16 v[88:91], v[4:7], v[8:11], v[88:91]
	s_waitcnt lgkmcnt(1)
	v_mfma_f32_16x16x32_f16 v[80:83], v[104:107], v[8:11], v[80:83]
	s_waitcnt lgkmcnt(0)
	v_mfma_f32_16x16x32_f16 v[76:79], v[108:111], v[8:11], v[28:31]
	s_setprio 1
	ds_read_b128 v[8:11], v98 offset:26624
	ds_read_b128 v[112:115], v98 offset:27648
	s_waitcnt vmcnt(3) lgkmcnt(0)
	s_barrier
	s_setprio 0
	v_mfma_f32_16x16x32_f16 v[72:75], v[0:3], v[12:15], v[72:75]
	v_mfma_f32_16x16x32_f16 v[68:71], v[4:7], v[12:15], v[68:71]
	s_mov_b32 m0, s40
	s_nop 0
	global_load_lds_dwordx4 v100, s[30:31]
	v_mfma_f32_16x16x32_f16 v[64:67], v[104:107], v[12:15], v[64:67]
	v_mfma_f32_16x16x32_f16 v[60:63], v[108:111], v[12:15], v[24:27]
	s_mov_b32 m0, s41
	s_nop 0
	global_load_lds_dwordx4 v99, s[30:31]
	s_add_i32 s13, s13, 2
	s_add_u32 s14, s14, 0x100000
	s_addc_u32 s15, s15, 0
	s_add_u32 s20, s20, s16
	s_addc_u32 s21, s21, s17
	s_waitcnt lgkmcnt(1)
	v_mfma_f32_16x16x32_f16 v[56:59], v[0:3], v[8:11], v[56:59]
	v_mfma_f32_16x16x32_f16 v[44:47], v[108:111], v[8:11], v[16:19]
	s_mov_b32 m0, s48
	s_nop 0
	global_load_lds_dwordx4 v102, s[34:35]
	s_cmp_gt_u32 s13, 25
	s_setprio 1
	ds_read_b128 v[28:31], v164
	ds_read_b128 v[24:27], v164 offset:1024
	s_nop 0
	ds_read_b128 v[16:19], v164 offset:2048
	s_waitcnt lgkmcnt(3)
	v_mfma_f32_16x16x32_f16 v[40:43], v[0:3], v[112:115], v[20:23]
	s_setprio 1
	ds_read_b128 v[0:3], v164 offset:3072
	s_nop 1
	ds_read_b128 v[20:23], v165 offset:16384
	ds_read_b128 v[12:15], v165 offset:17408
	v_mfma_f32_16x16x32_f16 v[48:51], v[4:7], v[8:11], v[48:51]
	v_mfma_f32_16x16x32_f16 v[52:55], v[104:107], v[8:11], v[52:55]
	v_mfma_f32_16x16x32_f16 v[36:39], v[4:7], v[112:115], v[36:39]
	s_setprio 1
	ds_read_b128 v[8:11], v165 offset:18432
	ds_read_b128 v[4:7], v165 offset:19456
	v_mfma_f32_16x16x32_f16 v[32:35], v[104:107], v[112:115], v[32:35]
	v_mfma_f32_16x16x32_f16 v[84:87], v[108:111], v[112:115], v[84:87]
	s_cbranch_scc1 .Lout_exit
	s_waitcnt vmcnt(3) lgkmcnt(0)
	s_barrier
	s_setprio 0
	s_add_u32 s34, s20, s28
	s_addc_u32 s35, s21, s27
	s_waitcnt lgkmcnt(3)
	v_mfma_f32_16x16x32_f16 v[92:95], v[20:23], v[28:31], v[92:95]
	v_mfma_f32_16x16x32_f16 v[72:75], v[20:23], v[24:27], v[72:75]
	s_mov_b32 m0, s42
	s_nop 0
	global_load_lds_dwordx4 v100, s[14:15]
	v_mfma_f32_16x16x32_f16 v[56:59], v[20:23], v[16:19], v[56:59]
	v_mfma_f32_16x16x32_f16 v[20:23], v[20:23], v[0:3], v[40:43]
	s_mov_b32 m0, s43
	s_nop 0
	global_load_lds_dwordx4 v99, s[14:15]
	s_waitcnt lgkmcnt(2)
	v_mfma_f32_16x16x32_f16 v[88:91], v[12:15], v[28:31], v[88:91]
	s_mov_b32 m0, s49
	s_nop 0
	global_load_lds_dwordx4 v102, s[34:35]
	s_waitcnt lgkmcnt(1)
	v_mfma_f32_16x16x32_f16 v[80:83], v[8:11], v[28:31], v[80:83]
	s_waitcnt lgkmcnt(0)
	v_mfma_f32_16x16x32_f16 v[28:31], v[4:7], v[28:31], v[76:79]
	s_add_u32 s30, s14, 0x80000
	s_addc_u32 s31, s15, 0
	s_add_u32 s34, s20, s18
	v_mfma_f32_16x16x32_f16 v[68:71], v[12:15], v[24:27], v[68:71]
	s_addc_u32 s35, s21, s19
	v_mfma_f32_16x16x32_f16 v[64:67], v[8:11], v[24:27], v[64:67]
	v_mfma_f32_16x16x32_f16 v[24:27], v[4:7], v[24:27], v[60:63]
	v_mfma_f32_16x16x32_f16 v[48:51], v[12:15], v[16:19], v[48:51]
	v_mfma_f32_16x16x32_f16 v[52:55], v[8:11], v[16:19], v[52:55]
	v_mfma_f32_16x16x32_f16 v[16:19], v[4:7], v[16:19], v[44:47]
	v_mfma_f32_16x16x32_f16 v[36:39], v[12:15], v[0:3], v[36:39]
	v_mfma_f32_16x16x32_f16 v[32:35], v[8:11], v[0:3], v[32:35]
	v_mfma_f32_16x16x32_f16 v[84:87], v[4:7], v[0:3], v[84:87]
	s_setprio 1
	ds_read_b128 v[0:3], v165 offset:40960
	ds_read_b128 v[4:7], v165 offset:41984
	ds_read_b128 v[8:11], v164 offset:24576
	ds_read_b128 v[12:15], v164 offset:25600
	ds_read_b128 v[104:107], v165 offset:43008
	ds_read_b128 v[108:111], v165 offset:44032
	s_waitcnt lgkmcnt(3)
	v_mfma_f32_16x16x32_f16 v[92:95], v[0:3], v[8:11], v[92:95]
	v_mfma_f32_16x16x32_f16 v[88:91], v[4:7], v[8:11], v[88:91]
	s_waitcnt lgkmcnt(1)
	v_mfma_f32_16x16x32_f16 v[80:83], v[104:107], v[8:11], v[80:83]
	s_waitcnt lgkmcnt(0)
	v_mfma_f32_16x16x32_f16 v[76:79], v[108:111], v[8:11], v[28:31]
	s_setprio 1
	ds_read_b128 v[8:11], v164 offset:26624
	ds_read_b128 v[112:115], v164 offset:27648
	s_waitcnt vmcnt(3) lgkmcnt(0)
	s_barrier
	s_setprio 0
	v_mfma_f32_16x16x32_f16 v[72:75], v[0:3], v[12:15], v[72:75]
	v_mfma_f32_16x16x32_f16 v[68:71], v[4:7], v[12:15], v[68:71]
	s_mov_b32 m0, s44
	s_nop 0
	global_load_lds_dwordx4 v100, s[30:31]
	v_mfma_f32_16x16x32_f16 v[64:67], v[104:107], v[12:15], v[64:67]
	v_mfma_f32_16x16x32_f16 v[60:63], v[108:111], v[12:15], v[24:27]
	s_mov_b32 m0, s45
	s_nop 0
	global_load_lds_dwordx4 v99, s[30:31]
	s_add_i32 s13, s13, 2
	s_add_u32 s14, s14, 0x100000
	s_addc_u32 s15, s15, 0
	s_add_u32 s20, s20, s16
	s_addc_u32 s21, s21, s17
	s_waitcnt lgkmcnt(1)
	v_mfma_f32_16x16x32_f16 v[56:59], v[0:3], v[8:11], v[56:59]
	v_mfma_f32_16x16x32_f16 v[44:47], v[108:111], v[8:11], v[16:19]
	s_mov_b32 m0, s50
	s_nop 0
	global_load_lds_dwordx4 v102, s[34:35]
	s_cmp_gt_u32 s13, 25
	s_setprio 1
	ds_read_b128 v[28:31], v98
	ds_read_b128 v[24:27], v98 offset:1024
	s_nop 0
	ds_read_b128 v[16:19], v98 offset:2048
	s_waitcnt lgkmcnt(3)
	v_mfma_f32_16x16x32_f16 v[40:43], v[0:3], v[112:115], v[20:23]
	s_setprio 1
	ds_read_b128 v[0:3], v98 offset:3072
	s_nop 1
	ds_read_b128 v[20:23], v103 offset:16384
	ds_read_b128 v[12:15], v103 offset:17408
	v_mfma_f32_16x16x32_f16 v[48:51], v[4:7], v[8:11], v[48:51]
	v_mfma_f32_16x16x32_f16 v[52:55], v[104:107], v[8:11], v[52:55]
	v_mfma_f32_16x16x32_f16 v[36:39], v[4:7], v[112:115], v[36:39]
	s_setprio 1
	ds_read_b128 v[8:11], v103 offset:18432
	ds_read_b128 v[4:7], v103 offset:19456
	v_mfma_f32_16x16x32_f16 v[32:35], v[104:107], v[112:115], v[32:35]
	v_mfma_f32_16x16x32_f16 v[84:87], v[108:111], v[112:115], v[84:87]
	s_cbranch_scc0 .Lout_P
